# attention phase: waves 4..7 no longer run at raised static priority (all waves equal)
# baseline (speedup 1.0000x reference)
; #define LAS __attribute__((address_space(3)))
; __global__ void __launch_bounds__(NTHREADS, 2) fwd_kernel(Args args) {
;     ...
;         for (int i = tid; i < 16 * 132; i += NTHREADS) lut[i] = ((const float*)(ws + WS_TAB + TAB_LUT))[i];
;         __syncthreads();
;         if ((tid >> 6) >= 4) __builtin_amdgcn_s_setprio(2);
;         for (int i = 0; i < 16; ++i) { const int bg = 8 * (i >> 2) + ((int)blockIdx.x & 7), wi = (int)blockIdx.x >> 3, k = i & 3;
;             const int tau = k == 0 ? wi : k == 1 ? 63 - wi : k == 2 ? 64 + wi : 127 - wi;
;             if (k == 0) {
;                 __syncthreads();
;                 LAS float* nbt = (LAS float*)(lds + NB_OFF);
;                 for (int x = tid; x < 16 * 264; x += NTHREADS) { const int rr = x / 1056, sh = (x / 264) & 3, z = x % 264, d = 196 - z - sh;
;                     nbt[x] = d < 0 ? -__builtin_inff() : lut[((bg & 3) * 4 + rr) * 132 + (d > 128 ? 128 : d)]; }
;                 __syncthreads();
;             }
;             nsa_unit(ws, lds, lut, bg >> 2, bg & 3, tau, tid); }
.LBB0_1015:
	global_load_dword v6, v[2:3], off
	v_add_u32_e32 v4, 0x200, v4
	v_cmp_lt_u32_e32 vcc, s0, v4
	v_lshl_add_u64 v[2:3], v[2:3], 0, s[10:11]
	s_or_b64 s[8:9], vcc, s[8:9]
	s_waitcnt vmcnt(0)
	ds_write_b32 v5, v6
	v_add_u32_e32 v5, 0x800, v5
	s_andn2_b64 exec, exec, s[8:9]
	s_cbranch_execnz .LBB0_1015
	v_writelane_b32 v253, s2, 20
	s_nop 1
	v_writelane_b32 v253, s3, 21
	s_or_b64 exec, exec, s[8:9]
	s_movk_i32 s0, 0xff
	v_cmp_lt_u32_e32 vcc, s0, v0
	s_waitcnt lgkmcnt(0)
	s_barrier
	s_and_saveexec_b64 s[8:9], vcc
	s_setprio 0
	s_or_b64 exec, exec, s[8:9]
	v_readlane_b32 s2, v253, 11
	s_ashr_i32 s82, s2, 3
	s_add_i32 s0, s82, 64
	v_writelane_b32 v253, s0, 22
	s_sub_i32 s0, 0x7f, s82
	v_writelane_b32 v253, s0, 26
	s_sub_i32 s0, 63, s82
	s_and_b32 s52, s2, 3
	v_writelane_b32 v253, s0, 28
	s_lshl_b32 s0, s2, 2
	s_and_b32 s35, s2, 4
	s_and_b32 s74, s0, 12
	s_lshl_b32 s89, s52, 2
	s_add_u32 s87, s6, 0xd800000
	s_addc_u32 s90, s7, 0
	s_lshl_b32 s78, s52, 7
	s_add_u32 s0, s6, 0x37600000
	v_writelane_b32 v253, s0, 29
	s_addc_u32 s0, s7, 0
	v_writelane_b32 v253, s0, 30
	s_add_u32 s0, s6, s78
	s_addc_u32 s1, s7, 0
	s_add_u32 s3, s0, 0x37400000
	v_writelane_b32 v253, s3, 31
	s_addc_u32 s3, s1, 0
	v_writelane_b32 v253, s3, 32
	s_add_u32 s3, s6, 0x19800000
	v_writelane_b32 v253, s3, 34
	s_addc_u32 s3, s7, 0
	v_writelane_b32 v253, s3, 35
	s_add_u32 s3, s6, 0x1b800000
	v_writelane_b32 v253, s3, 36
	s_addc_u32 s3, s7, 0
	s_add_u32 s28, s6, 0x31800000
	s_addc_u32 s29, s7, 0
	v_writelane_b32 v253, s3, 37
	s_add_u32 s3, s6, 0x1d800000
	v_writelane_b32 v253, s3, 38
	s_addc_u32 s3, s7, 0
	v_writelane_b32 v253, s3, 39
	s_add_u32 s3, s6, 0x1f800000
	v_writelane_b32 v253, s3, 40
	s_addc_u32 s3, s7, 0
	s_add_u32 s30, s6, 0x31800004
	s_addc_u32 s31, s7, 0
	s_add_u32 s40, s6, 0x31800008
	s_addc_u32 s41, s7, 0
	s_add_u32 s42, s6, 0x1800000
	s_addc_u32 s43, s7, 0
	v_writelane_b32 v253, s3, 41
	s_add_u32 s3, s0, 0x37408000
	v_writelane_b32 v253, s3, 42
	s_addc_u32 s3, s1, 0
	s_lshl_b32 s2, s2, 16
	v_writelane_b32 v253, s3, 44
	s_and_b32 s2, s2, 0x40000
	v_writelane_b32 v253, s2, 46
	s_add_u32 s2, s6, 0x37600080
	s_addc_u32 s3, s7, 0
	s_or_b32 s94, s35, s52
	s_add_u32 s95, s0, 0x19810000
	s_addc_u32 s96, s1, 0
	s_add_u32 s97, s6, 0x1b800100
	v_writelane_b32 v253, s2, 47
	s_addc_u32 s4, s7, 0
	s_add_u32 s0, s0, 0x1d7c8000
	v_writelane_b32 v253, s3, 48
	v_writelane_b32 v253, s0, 49
	s_addc_u32 s0, s1, 0
	v_writelane_b32 v253, s0, 50
	s_add_u32 s0, s6, 0x1f7ffc80
	v_writelane_b32 v253, s0, 51
	s_addc_u32 s0, s7, 0
	v_add_u32_e32 v151, 0x23d40, v1
	v_writelane_b32 v253, s0, 53
	s_add_i32 s25, 0, 0x20c00
	v_mbcnt_lo_u32_b32 v1, -1, 0
	s_add_i32 s1, 0, 0x24040
	s_mov_b32 s27, 0
	s_movk_i32 s56, 0x200
	v_mov_b32_e32 v153, 0
	s_add_i32 s57, 0, 0x20850
	s_add_i32 s34, 0, 0x20854
	s_mov_b64 s[46:47], 0x8000
	s_mov_b64 s[48:49], 0x80
	v_mbcnt_hi_u32_b32 v176, -1, v1
	s_movk_i32 s0, 0xc0
	v_writelane_b32 v253, s1, 54
	s_mov_b32 s20, 0x3f803f80
	s_mov_b32 s54, 0x7cf0bdc2
	v_mov_b32_e32 v177, 1
	s_add_i32 s1, 0, 0x23840
	v_mov_b32_e32 v178, 3
	v_mov_b32_e32 v179, s25
	v_mov_b32_e32 v180, 0x80
	v_mov_b32_e32 v2, 0xff800000
	v_mov_b32_e32 v181, 0x100000
	v_mov_b32_e32 v182, 0x41
	s_mov_b32 s80, 0
	s_mov_b32 s81, 0
	v_writelane_b32 v253, s1, 56
	s_branch .LBB0_1021
